# as previous but static s_setprio 1 for waves 0-3 (older half) instead
# speedup vs baseline: 1.0214x; 1.0029x over previous
_Z10fwd_kernel6Params:
	s_mov_b64 s[88:89], s[0:1]
	v_readfirstlane_b32 s3, v0
	s_nop 3
	s_lshr_b32 s3, s3, 6
	s_cmp_lt_u32 s3, 4
	s_cbranch_scc0 .Lprio_done
	s_setprio 1
